# arrival wait relaxed to vmcnt(1): the L1 invalidate issued behind the arrival stays in flight while the last arrival writes the L2 back
# baseline (speedup 1.0000x reference)
; __device__ __forceinline__ unsigned xb_ld(unsigned* p)              { return __hip_atomic_load(p, __ATOMIC_RELAXED, __HIP_MEMORY_SCOPE_AGENT); }
; __device__ __forceinline__ unsigned xb_add(unsigned* p, unsigned v) { return __hip_atomic_fetch_add(p, v, __ATOMIC_RELAXED, __HIP_MEMORY_SCOPE_AGENT); }
; #define XB_SPIN(cond, bar) do { unsigned _sp = 0; while (cond) { __builtin_amdgcn_s_sleep(1); \
;     if ((++_sp & 255u) == 0u) { if (xb_ld(&(bar)[XB_TMO])) break; if (_sp > XB_SPIN_CAP) { atomicAdd(&(bar)[XB_TMO], 1u); break; } } } } while (0)
; __device__ __forceinline__ void xcd_barrier(const XcdBarrier& b, const int tid) {
;     ...
;         const unsigned old = xb_add(&bar[XB_XSUB(b.x)], 1u);
;         const unsigned gen = old / nloc;
;         if (old + 1u == (gen + 1u) * nloc) {
;             __builtin_amdgcn_fence(__ATOMIC_RELEASE, "agent");
;             asm volatile("s_waitcnt vmcnt(0)" ::: "memory");
;             const unsigned og = xb_add(&bar[XB_TOP], 1u);
;             const unsigned tg = og / nx;
;             if (og + 1u == (tg + 1u) * nx) xb_add(&bar[XB_TOPGEN], 1u);
;             else XB_SPIN(xb_ld(&bar[XB_TOPGEN]) == tg, bar);
.LBB0_79:
	s_or_b64 exec, exec, s[16:17]
	buffer_inv sc1
	v_cvt_f32_u32_e32 v4, v2
	s_waitcnt vmcnt(1)
	v_readfirstlane_b32 s12, v3
	v_sub_u32_e32 v3, 0, v2
	v_rcp_iflag_f32_e32 v4, v4
	v_add_u32_e32 v5, s12, v1
	v_mul_f32_e32 v4, 0x4f7ffffe, v4
	v_cvt_u32_f32_e32 v4, v4
	v_mul_lo_u32 v1, v3, v4
	v_mul_hi_u32 v1, v4, v1
	v_add_u32_e32 v1, v4, v1
	v_mul_hi_u32 v1, v5, v1
	v_mul_lo_u32 v3, v1, v2
	v_sub_u32_e32 v3, v5, v3
	v_add_u32_e32 v4, 1, v1
	v_cmp_ge_u32_e32 vcc, v3, v2
	s_nop 1
	v_cndmask_b32_e32 v1, v1, v4, vcc
	v_sub_u32_e32 v4, v3, v2
	v_cndmask_b32_e32 v3, v3, v4, vcc
	v_add_u32_e32 v4, 1, v1
	v_cmp_ge_u32_e32 vcc, v3, v2
	v_add_u32_e32 v3, 1, v5
	s_nop 0
	v_cndmask_b32_e32 v1, v1, v4, vcc
	v_mul_lo_u32 v4, v2, v1
	v_add_u32_e32 v2, v4, v2
	s_waitcnt lgkmcnt(0)
	v_add_u32_e32 v4, 1, v1
	v_mul_lo_u32 v4, v4, v0
	v_mov_b32_e32 v5, 0x3600
	v_cmp_ne_u32_e32 vcc, v3, v2
	s_cbranch_vccnz .Lgb0_wait
	buffer_wbl2 sc1
	s_waitcnt vmcnt(0) lgkmcnt(0)
	v_mov_b32_e32 v2, 1
	global_atomic_add v5, v2, s[26:27]
	global_atomic_add v5, v2, s[26:27] offset:256
	global_atomic_add v5, v2, s[26:27] offset:512
	global_atomic_add v5, v2, s[26:27] offset:768
	global_atomic_add v5, v2, s[26:27] offset:1024
	global_atomic_add v5, v2, s[26:27] offset:1280
	global_atomic_add v5, v2, s[26:27] offset:1536
	global_atomic_add v5, v2, s[26:27] offset:1792

; __device__ __forceinline__ unsigned xb_ld(unsigned* p)              { return __hip_atomic_load(p, __ATOMIC_RELAXED, __HIP_MEMORY_SCOPE_AGENT); }
; __device__ __forceinline__ unsigned xb_add(unsigned* p, unsigned v) { return __hip_atomic_fetch_add(p, v, __ATOMIC_RELAXED, __HIP_MEMORY_SCOPE_AGENT); }
; #define XB_SPIN(cond, bar) do { unsigned _sp = 0; while (cond) { __builtin_amdgcn_s_sleep(1); \
;     if ((++_sp & 255u) == 0u) { if (xb_ld(&(bar)[XB_TMO])) break; if (_sp > XB_SPIN_CAP) { atomicAdd(&(bar)[XB_TMO], 1u); break; } } } } while (0)
; __device__ __forceinline__ void xcd_barrier(const XcdBarrier& b, const int tid) {
;     ...
;         const unsigned old = xb_add(&bar[XB_XSUB(b.x)], 1u);
;         const unsigned gen = old / nloc;
;         if (old + 1u == (gen + 1u) * nloc) {
;             __builtin_amdgcn_fence(__ATOMIC_RELEASE, "agent");
;             asm volatile("s_waitcnt vmcnt(0)" ::: "memory");
;             const unsigned og = xb_add(&bar[XB_TOP], 1u);
;             const unsigned tg = og / nx;
;             if (og + 1u == (tg + 1u) * nx) xb_add(&bar[XB_TOPGEN], 1u);
;             else XB_SPIN(xb_ld(&bar[XB_TOPGEN]) == tg, bar);
.LBB0_169:
	s_or_b64 exec, exec, s[22:23]
	buffer_inv sc1
	v_cvt_f32_u32_e32 v4, v2
	s_waitcnt vmcnt(1)
	v_readfirstlane_b32 s20, v3
	v_sub_u32_e32 v3, 0, v2
	v_rcp_iflag_f32_e32 v4, v4
	v_add_u32_e32 v5, s20, v1
	v_mul_f32_e32 v4, 0x4f7ffffe, v4
	v_cvt_u32_f32_e32 v4, v4
	v_mul_lo_u32 v1, v3, v4
	v_mul_hi_u32 v1, v4, v1
	v_add_u32_e32 v1, v4, v1
	v_mul_hi_u32 v1, v5, v1
	v_mul_lo_u32 v3, v1, v2
	v_sub_u32_e32 v3, v5, v3
	v_add_u32_e32 v4, 1, v1
	v_cmp_ge_u32_e32 vcc, v3, v2
	s_nop 1
	v_cndmask_b32_e32 v1, v1, v4, vcc
	v_sub_u32_e32 v4, v3, v2
	v_cndmask_b32_e32 v3, v3, v4, vcc
	v_add_u32_e32 v4, 1, v1
	v_cmp_ge_u32_e32 vcc, v3, v2
	v_add_u32_e32 v3, 1, v5
	s_nop 0
	v_cndmask_b32_e32 v1, v1, v4, vcc
	v_mul_lo_u32 v4, v2, v1
	v_add_u32_e32 v2, v4, v2
	s_waitcnt lgkmcnt(0)
	v_add_u32_e32 v4, 1, v1
	v_mul_lo_u32 v4, v4, v0
	v_mov_b32_e32 v5, 0x3600
	v_cmp_ne_u32_e32 vcc, v3, v2
	s_cbranch_vccnz .Lgb1_out
	buffer_wbl2 sc1
	s_waitcnt vmcnt(0) lgkmcnt(0)
	v_mov_b32_e32 v2, 1
	global_atomic_add v5, v2, s[26:27]
	global_atomic_add v5, v2, s[26:27] offset:256
	global_atomic_add v5, v2, s[26:27] offset:512
	global_atomic_add v5, v2, s[26:27] offset:768
	global_atomic_add v5, v2, s[26:27] offset:1024
	global_atomic_add v5, v2, s[26:27] offset:1280
	global_atomic_add v5, v2, s[26:27] offset:1536
	global_atomic_add v5, v2, s[26:27] offset:1792

; __device__ __forceinline__ unsigned xb_ld(unsigned* p)              { return __hip_atomic_load(p, __ATOMIC_RELAXED, __HIP_MEMORY_SCOPE_AGENT); }
; __device__ __forceinline__ unsigned xb_add(unsigned* p, unsigned v) { return __hip_atomic_fetch_add(p, v, __ATOMIC_RELAXED, __HIP_MEMORY_SCOPE_AGENT); }
; #define XB_SPIN(cond, bar) do { unsigned _sp = 0; while (cond) { __builtin_amdgcn_s_sleep(1); \
;     if ((++_sp & 255u) == 0u) { if (xb_ld(&(bar)[XB_TMO])) break; if (_sp > XB_SPIN_CAP) { atomicAdd(&(bar)[XB_TMO], 1u); break; } } } } while (0)
; __device__ __forceinline__ void xcd_barrier(const XcdBarrier& b, const int tid) {
;     ...
;         const unsigned old = xb_add(&bar[XB_XSUB(b.x)], 1u);
;         const unsigned gen = old / nloc;
;         if (old + 1u == (gen + 1u) * nloc) {
;             __builtin_amdgcn_fence(__ATOMIC_RELEASE, "agent");
;             asm volatile("s_waitcnt vmcnt(0)" ::: "memory");
;             const unsigned og = xb_add(&bar[XB_TOP], 1u);
;             const unsigned tg = og / nx;
;             if (og + 1u == (tg + 1u) * nx) xb_add(&bar[XB_TOPGEN], 1u);
;             else XB_SPIN(xb_ld(&bar[XB_TOPGEN]) == tg, bar);
.LBB0_433:
	s_or_b64 exec, exec, s[12:13]
	buffer_inv sc1
	v_cvt_f32_u32_e32 v4, v2
	s_waitcnt vmcnt(1)
	v_readfirstlane_b32 s6, v3
	v_sub_u32_e32 v3, 0, v2
	v_rcp_iflag_f32_e32 v4, v4
	v_add_u32_e32 v5, s6, v1
	v_mul_f32_e32 v4, 0x4f7ffffe, v4
	v_cvt_u32_f32_e32 v4, v4
	v_mul_lo_u32 v1, v3, v4
	v_mul_hi_u32 v1, v4, v1
	v_add_u32_e32 v1, v4, v1
	v_mul_hi_u32 v1, v5, v1
	v_mul_lo_u32 v3, v1, v2
	v_sub_u32_e32 v3, v5, v3
	v_add_u32_e32 v4, 1, v1
	v_cmp_ge_u32_e32 vcc, v3, v2
	s_nop 1
	v_cndmask_b32_e32 v1, v1, v4, vcc
	v_sub_u32_e32 v4, v3, v2
	v_cndmask_b32_e32 v3, v3, v4, vcc
	v_add_u32_e32 v4, 1, v1
	v_cmp_ge_u32_e32 vcc, v3, v2
	v_add_u32_e32 v3, 1, v5
	s_nop 0
	v_cndmask_b32_e32 v1, v1, v4, vcc
	v_mul_lo_u32 v4, v2, v1
	v_add_u32_e32 v2, v4, v2
	s_waitcnt lgkmcnt(0)
	v_add_u32_e32 v4, 1, v1
	v_mul_lo_u32 v4, v4, v0
	v_mov_b32_e32 v5, 0x3600
	v_cmp_ne_u32_e32 vcc, v3, v2
	s_cbranch_vccnz .Lgb2_wait
	buffer_wbl2 sc1
	s_waitcnt vmcnt(0) lgkmcnt(0)
	v_mov_b32_e32 v2, 1
	global_atomic_add v5, v2, s[26:27]
	global_atomic_add v5, v2, s[26:27] offset:256
	global_atomic_add v5, v2, s[26:27] offset:512
	global_atomic_add v5, v2, s[26:27] offset:768
	global_atomic_add v5, v2, s[26:27] offset:1024
	global_atomic_add v5, v2, s[26:27] offset:1280
	global_atomic_add v5, v2, s[26:27] offset:1536
	global_atomic_add v5, v2, s[26:27] offset:1792

; __device__ __forceinline__ unsigned xb_ld(unsigned* p)              { return __hip_atomic_load(p, __ATOMIC_RELAXED, __HIP_MEMORY_SCOPE_AGENT); }
; __device__ __forceinline__ unsigned xb_add(unsigned* p, unsigned v) { return __hip_atomic_fetch_add(p, v, __ATOMIC_RELAXED, __HIP_MEMORY_SCOPE_AGENT); }
; #define XB_SPIN(cond, bar) do { unsigned _sp = 0; while (cond) { __builtin_amdgcn_s_sleep(1); \
;     if ((++_sp & 255u) == 0u) { if (xb_ld(&(bar)[XB_TMO])) break; if (_sp > XB_SPIN_CAP) { atomicAdd(&(bar)[XB_TMO], 1u); break; } } } } while (0)
; __device__ __forceinline__ void xcd_barrier(const XcdBarrier& b, const int tid) {
;     ...
;         const unsigned old = xb_add(&bar[XB_XSUB(b.x)], 1u);
;         const unsigned gen = old / nloc;
;         if (old + 1u == (gen + 1u) * nloc) {
;             __builtin_amdgcn_fence(__ATOMIC_RELEASE, "agent");
;             asm volatile("s_waitcnt vmcnt(0)" ::: "memory");
;             const unsigned og = xb_add(&bar[XB_TOP], 1u);
;             const unsigned tg = og / nx;
;             if (og + 1u == (tg + 1u) * nx) xb_add(&bar[XB_TOPGEN], 1u);
;             else XB_SPIN(xb_ld(&bar[XB_TOPGEN]) == tg, bar);
.LBB0_512:
	s_or_b64 exec, exec, s[8:9]
	buffer_inv sc1
	v_cvt_f32_u32_e32 v4, v2
	s_waitcnt vmcnt(1)
	v_readfirstlane_b32 s6, v3
	v_sub_u32_e32 v3, 0, v2
	v_rcp_iflag_f32_e32 v4, v4
	v_add_u32_e32 v5, s6, v1
	v_mul_f32_e32 v4, 0x4f7ffffe, v4
	v_cvt_u32_f32_e32 v4, v4
	v_mul_lo_u32 v1, v3, v4
	v_mul_hi_u32 v1, v4, v1
	v_add_u32_e32 v1, v4, v1
	v_mul_hi_u32 v1, v5, v1
	v_mul_lo_u32 v3, v1, v2
	v_sub_u32_e32 v3, v5, v3
	v_add_u32_e32 v4, 1, v1
	v_cmp_ge_u32_e32 vcc, v3, v2
	s_nop 1
	v_cndmask_b32_e32 v1, v1, v4, vcc
	v_sub_u32_e32 v4, v3, v2
	v_cndmask_b32_e32 v3, v3, v4, vcc
	v_add_u32_e32 v4, 1, v1
	v_cmp_ge_u32_e32 vcc, v3, v2
	v_add_u32_e32 v3, 1, v5
	s_nop 0
	v_cndmask_b32_e32 v1, v1, v4, vcc
	v_mul_lo_u32 v4, v2, v1
	v_add_u32_e32 v2, v4, v2
	s_waitcnt lgkmcnt(0)
	v_add_u32_e32 v4, 1, v1
	v_mul_lo_u32 v4, v4, v0
	v_mov_b32_e32 v5, 0x3600
	v_cmp_ne_u32_e32 vcc, v3, v2
	s_cbranch_vccnz .Lgb3_wait
	buffer_wbl2 sc1
	s_waitcnt vmcnt(0) lgkmcnt(0)
	v_mov_b32_e32 v2, 1
	global_atomic_add v5, v2, s[26:27]
	global_atomic_add v5, v2, s[26:27] offset:256
	global_atomic_add v5, v2, s[26:27] offset:512
	global_atomic_add v5, v2, s[26:27] offset:768
	global_atomic_add v5, v2, s[26:27] offset:1024
	global_atomic_add v5, v2, s[26:27] offset:1280
	global_atomic_add v5, v2, s[26:27] offset:1536
	global_atomic_add v5, v2, s[26:27] offset:1792

; __device__ __forceinline__ unsigned xb_ld(unsigned* p)              { return __hip_atomic_load(p, __ATOMIC_RELAXED, __HIP_MEMORY_SCOPE_AGENT); }
; __device__ __forceinline__ unsigned xb_add(unsigned* p, unsigned v) { return __hip_atomic_fetch_add(p, v, __ATOMIC_RELAXED, __HIP_MEMORY_SCOPE_AGENT); }
; #define XB_SPIN(cond, bar) do { unsigned _sp = 0; while (cond) { __builtin_amdgcn_s_sleep(1); \
;     if ((++_sp & 255u) == 0u) { if (xb_ld(&(bar)[XB_TMO])) break; if (_sp > XB_SPIN_CAP) { atomicAdd(&(bar)[XB_TMO], 1u); break; } } } } while (0)
; __device__ __forceinline__ void xcd_barrier(const XcdBarrier& b, const int tid) {
;     ...
;         const unsigned old = xb_add(&bar[XB_XSUB(b.x)], 1u);
;         const unsigned gen = old / nloc;
;         if (old + 1u == (gen + 1u) * nloc) {
;             __builtin_amdgcn_fence(__ATOMIC_RELEASE, "agent");
;             asm volatile("s_waitcnt vmcnt(0)" ::: "memory");
;             const unsigned og = xb_add(&bar[XB_TOP], 1u);
;             const unsigned tg = og / nx;
;             if (og + 1u == (tg + 1u) * nx) xb_add(&bar[XB_TOPGEN], 1u);
;             else XB_SPIN(xb_ld(&bar[XB_TOPGEN]) == tg, bar);
.LBB0_802:
	s_or_b64 exec, exec, s[10:11]
	buffer_inv sc1
	v_cvt_f32_u32_e32 v4, v2
	s_waitcnt vmcnt(1)
	v_readfirstlane_b32 s8, v3
	v_sub_u32_e32 v3, 0, v2
	v_rcp_iflag_f32_e32 v4, v4
	v_add_u32_e32 v5, s8, v1
	v_mul_f32_e32 v4, 0x4f7ffffe, v4
	v_cvt_u32_f32_e32 v4, v4
	v_mul_lo_u32 v1, v3, v4
	v_mul_hi_u32 v1, v4, v1
	v_add_u32_e32 v1, v4, v1
	v_mul_hi_u32 v1, v5, v1
	v_mul_lo_u32 v3, v1, v2
	v_sub_u32_e32 v3, v5, v3
	v_add_u32_e32 v4, 1, v1
	v_cmp_ge_u32_e32 vcc, v3, v2
	s_nop 1
	v_cndmask_b32_e32 v1, v1, v4, vcc
	v_sub_u32_e32 v4, v3, v2
	v_cndmask_b32_e32 v3, v3, v4, vcc
	v_add_u32_e32 v4, 1, v1
	v_cmp_ge_u32_e32 vcc, v3, v2
	v_add_u32_e32 v3, 1, v5
	s_nop 0
	v_cndmask_b32_e32 v1, v1, v4, vcc
	v_mul_lo_u32 v4, v2, v1
	v_add_u32_e32 v2, v4, v2
	s_waitcnt lgkmcnt(0)
	v_add_u32_e32 v4, 1, v1
	v_mul_lo_u32 v4, v4, v0
	v_mov_b32_e32 v5, 0x3600
	v_cmp_ne_u32_e32 vcc, v3, v2
	s_cbranch_vccnz .Lgb5_wait
	buffer_wbl2 sc1
	s_waitcnt vmcnt(0) lgkmcnt(0)
	v_mov_b32_e32 v2, 1
	global_atomic_add v5, v2, s[26:27]
	global_atomic_add v5, v2, s[26:27] offset:256
	global_atomic_add v5, v2, s[26:27] offset:512
	global_atomic_add v5, v2, s[26:27] offset:768
	global_atomic_add v5, v2, s[26:27] offset:1024
	global_atomic_add v5, v2, s[26:27] offset:1280
	global_atomic_add v5, v2, s[26:27] offset:1536
	global_atomic_add v5, v2, s[26:27] offset:1792
